# attention: Q fragments of the next 32-query sub-block prefetched one sub-block ahead (second register set + copy), first-tile waits no longer cover global loads
# speedup vs baseline: 1.0017x; 1.0017x over previous
; DI void phase_attn(const Frame& F, int j) {
;     ...
;             const int qrel = 32 * sub + r;
;             const size_t qrow = (size_t)(b * SEQ + q0 + qrel);
;             bf16x8 Qf[4];
; #pragma unroll
;             for (int s = 0; s < 4; ++s) Qf[s] = *(const bf16x8*)(QKV + qrow * QKV_N + head * 64 + 16 * s + 8 * h);
.LBB0_320:
	s_lshl_b32 s2, s82, 5
	v_or_b32_e32 v0, s2, v85
	v_or_b32_e32 v94, s9, v0
	v_mad_i64_i32 v[20:21], s[4:5], v94, s3, v[90:91]
	s_cmp_lg_u32 s82, 0
	s_cbranch_scc1 .Lattq_have
	global_load_dwordx4 v[152:155], v[20:21], off
	global_load_dwordx4 v[156:159], v[20:21], off offset:32
	global_load_dwordx4 v[160:163], v[20:21], off offset:64
	global_load_dwordx4 v[164:167], v[20:21], off offset:96
	s_waitcnt vmcnt(0)
	s_branch .Lattq_copy

; #define LAS __attribute__((address_space(3)))
; DI float kf(float c) { asm volatile("" : "+v"(c)); return c; }
; DI void phase_attn(const Frame& F, int j) {
;     ...
;             bf16x8 Qf[4];
; #pragma unroll
;             for (int s = 0; s < 4; ++s) Qf[s] = *(const bf16x8*)(QKV + qrow * QKV_N + head * 64 + 16 * s + 8 * h);
;             f32x16 O0, O1;
; #pragma unroll
;             for (int i = 0; i < 16; ++i) { O0[i] = 0.f; O1[i] = 0.f; }
;             float mrun = sink, lrun = h ? 0.f : 1.f;
;             for (int kt = sub; kt < sub + 9; ++kt) {
;                 f32x16 x;
; #pragma unroll
;                 for (int i = 0; i < 16; ++i) x[i] = 0.f;
; #pragma unroll
;                 for (int s = 0; s < 4; ++s) { const bf16x8 kf = *(const LAS bf16x8*)(Ks + (32 * kt + r) * KS_STRIDE + 16 * s + 8 * h);
;                     x = __builtin_amdgcn_mfma_f32_32x32x16_bf16(kf, Qf[s], x, 0, 0, 0); }
.Lattq_copy:
	v_mov_b32_e32 v48, v152
	v_mov_b32_e32 v49, v153
	v_mov_b32_e32 v50, v154
	v_mov_b32_e32 v51, v155
	v_mov_b32_e32 v52, v156
	v_mov_b32_e32 v53, v157
	v_mov_b32_e32 v54, v158
	v_mov_b32_e32 v55, v159
	v_mov_b32_e32 v56, v160
	v_mov_b32_e32 v57, v161
	v_mov_b32_e32 v58, v162
	v_mov_b32_e32 v59, v163
	v_mov_b32_e32 v60, v164
	v_mov_b32_e32 v61, v165
	v_mov_b32_e32 v62, v166
	v_mov_b32_e32 v63, v167
	s_cmp_lt_u32 s82, 3
	s_cbranch_scc0 .Lattq_nopf
	v_add_co_u32_e32 v168, vcc, 0x14000, v20
	s_nop 0
	v_addc_co_u32_e32 v169, vcc, 0, v21, vcc
	global_load_dwordx4 v[152:155], v[168:169], off
	global_load_dwordx4 v[156:159], v[168:169], off offset:32
	global_load_dwordx4 v[160:163], v[168:169], off offset:64
	global_load_dwordx4 v[164:167], v[168:169], off offset:96
.Lattq_nopf:
	v_mad_u64_u32 v[22:23], s[4:5], v0, s85, v[84:85]
	ds_read_b128 v[0:3], v22
	ds_read_b128 v[16:19], v22 offset:32
	v_or_b32_e32 v20, s2, v86
	v_lshlrev_b32_e32 v21, 1, v20
	v_add_u32_e32 v26, v113, v21
	s_waitcnt lgkmcnt(1)
	v_mfma_f32_32x32x16_bf16 v[0:15], v[0:3], v[48:51], 0
	s_waitcnt lgkmcnt(0)
	v_mfma_f32_32x32x16_bf16 v[0:15], v[16:19], v[52:55], v[0:15]
	ds_read_b128 v[16:19], v22 offset:64
	ds_read_b128 v[22:25], v22 offset:96
	s_waitcnt lgkmcnt(1)
	v_mfma_f32_32x32x16_bf16 v[0:15], v[16:19], v[56:59], v[0:15]
	v_add_u32_e32 v16, 0xd800, v26
	ds_read2_b64 v[44:47], v16 offset1:2
	ds_read2_b64 v[36:39], v16 offset0:4 offset1:6
	v_add_u32_e32 v16, v114, v21
	v_add_u32_e32 v16, 0x6000, v16
	ds_read2_b64 v[40:43], v16 offset0:64 offset1:66
	ds_read2_b64 v[32:35], v16 offset0:68 offset1:70
	s_waitcnt lgkmcnt(4)
	v_mfma_f32_32x32x16_bf16 v[0:15], v[22:25], v[60:63], v[0:15]
	s_add_i32 s4, s2, s31
	s_cmpk_lt_u32 s4, 0x1000
	s_cselect_b64 s[4:5], -1, 0
	s_add_i32 s6, s28, s2
	s_cmpk_lt_u32 s6, 0x1000
	s_cselect_b64 s[6:7], -1, 0
	s_add_i32 s2, s72, s2
	s_cmpk_lt_u32 s2, 0x1000
	s_cselect_b64 s[12:13], -1, 0
	ds_read_b32 v17, v134
	ds_read_b32 v16, v134 offset:4
	ds_read_b32 v19, v134 offset:8
	ds_read_b32 v18, v134 offset:12
	ds_read_b32 v22, v134 offset:32
	ds_read_b32 v21, v134 offset:36
	ds_read_b32 v24, v134 offset:40
	ds_read_b32 v23, v134 offset:44
	ds_read_b32 v26, v134 offset:64
	ds_read_b32 v25, v134 offset:68
	ds_read_b32 v27, v134 offset:72
	ds_read_b32 v64, v134 offset:76
	ds_read_b32 v66, v134 offset:96
	ds_read_b32 v65, v134 offset:100
	ds_read_b32 v68, v134 offset:104
	ds_read_b32 v67, v134 offset:108
	s_waitcnt lgkmcnt(0)
; DI float other_half(float x, int h) { const u32x2 r = __builtin_amdgcn_permlane32_swap(__builtin_bit_cast(unsigned, x), __builtin_bit_cast(unsigned, x), false, false); return __builtin_bit_cast(float, h ? r.x : r.y); }
; DI int crow(int reg, int h) { return (reg & 3) + 8 * (reg >> 2) + 4 * h; }
; DI void phase_attn(const Frame& F, int j) {
;     ...
;                 for (int i = 0; i < 16; ++i) { const int kl = 32 * kt + crow(i, h); const int rel = kl - 128 - qrel; const int kp = q0 - 128 + kl;
;                     const bool ok = rel >= -128 && rel <= 128 && kp >= 0 && kp < SEQ;
;                     const int bi = rel < -128 ? 0 : (rel > 128 ? 256 : rel + 128);
;                     const float sc = ok ? x[i] * (0.125f * 1.44269504f) + bT[hh * 260 + bi] : -1e30f; x[i] = sc; mt = fmaxf(mt, sc); }
;                 }
;                 mt = fmaxf(mt, other_half(mt, h));
;                 if (__builtin_amdgcn_ballot_w64(mt > mrun + 8.f) != 0) {
;                     const float mnew = fmaxf(mrun, mt); const float alpha = __builtin_amdgcn_exp2f(mrun - mnew); lrun *= alpha; mrun = mnew;
; #pragma unroll
;                     for (int i = 0; i < 16; ++i) { O0[i] *= alpha; O1[i] *= alpha; } }
;                 float ps = 0.f;
; #pragma unroll
;                 for (int i = 0; i < 16; ++i) { const float p = __builtin_amdgcn_exp2f(x[i] - mrun); x[i] = p; ps += p; }
;                 lrun += ps;
; #pragma unroll
;                 for (int s = 0; s < 2; ++s) { const bf16x8 pf = pack_step(x, s);
;                     const bf16x8 v0 = __builtin_shufflevector(vf[s][0], vf[s][1], 0, 1, 2, 3, 4, 5, 6, 7), v1 = __builtin_shufflevector(vf[s][2], vf[s][3], 0, 1, 2, 3, 4, 5, 6, 7);
;                     O0 = __builtin_amdgcn_mfma_f32_32x32x16_bf16(v0, pf, O0, 0, 0, 0);
;                     O1 = __builtin_amdgcn_mfma_f32_32x32x16_bf16(v1, pf, O1, 0, 0, 0); }
	v_fmac_f32_e32 v17, 0x3e38aa3b, v0
	v_fmac_f32_e32 v16, 0x3e38aa3b, v1
	v_fmac_f32_e32 v19, 0x3e38aa3b, v2
	v_fmac_f32_e32 v18, 0x3e38aa3b, v3
	v_fmac_f32_e32 v22, 0x3e38aa3b, v4
	v_fmac_f32_e32 v21, 0x3e38aa3b, v5
	v_fmac_f32_e32 v24, 0x3e38aa3b, v6
	v_fmac_f32_e32 v23, 0x3e38aa3b, v7
	v_fmac_f32_e32 v26, 0x3e38aa3b, v8
	v_fmac_f32_e32 v25, 0x3e38aa3b, v9
	v_fmac_f32_e32 v27, 0x3e38aa3b, v10
	v_fmac_f32_e32 v64, 0x3e38aa3b, v11
	v_fmac_f32_e32 v66, 0x3e38aa3b, v12
	v_fmac_f32_e32 v65, 0x3e38aa3b, v13
	v_fmac_f32_e32 v68, 0x3e38aa3b, v14
	v_fmac_f32_e32 v67, 0x3e38aa3b, v15
	v_mov_b32_e32 v1, 0xf149f2ca
	s_and_b64 vcc, s[38:39], s[4:5]
	v_cndmask_b32_e32 v17, v1, v17, vcc
	s_and_b64 vcc, s[46:47], s[6:7]
	v_cndmask_b32_e32 v22, v1, v22, vcc
	s_and_b64 vcc, s[54:55], s[4:5]
	v_cndmask_b32_e32 v26, v1, v26, vcc
	s_and_b64 vcc, s[62:63], s[12:13]
	v_cndmask_b32_e32 v66, v1, v66, vcc
	v_add_u32_e32 v2, s90, v20
	v_add_u32_e32 v3, s91, v20
	v_add_u32_e32 v4, s10, v20
	v_cmp_gt_u32_e64 s[4:5], s11, v2
	v_cmp_gt_u32_e64 s[6:7], s11, v3
	v_cmp_gt_u32_e64 s[12:13], s11, v4
	s_and_b64 s[4:5], s[40:41], s[4:5]
	s_and_b64 s[6:7], s[42:43], s[6:7]
	s_and_b64 s[12:13], s[44:45], s[12:13]
	v_cndmask_b32_e64 v16, v1, v16, s[4:5]
	v_cndmask_b32_e64 v19, v1, v19, s[6:7]
	v_cndmask_b32_e64 v18, v1, v18, s[12:13]
	v_add_u32_e32 v2, s74, v20
	v_add_u32_e32 v3, s75, v20
	v_add_u32_e32 v4, s76, v20
	v_cmp_gt_u32_e64 s[4:5], s11, v2
	v_cmp_gt_u32_e64 s[6:7], s11, v3
	v_cmp_gt_u32_e64 s[12:13], s11, v4
	s_and_b64 s[4:5], s[48:49], s[4:5]
	s_and_b64 s[6:7], s[50:51], s[6:7]
	s_and_b64 s[12:13], s[52:53], s[12:13]
	v_cndmask_b32_e64 v21, v1, v21, s[4:5]
	v_cndmask_b32_e64 v24, v1, v24, s[6:7]
	v_cndmask_b32_e64 v23, v1, v23, s[12:13]
	v_add_u32_e32 v2, s77, v20
	v_add_u32_e32 v3, s80, v20
	v_add_u32_e32 v4, s81, v20
	v_cmp_gt_u32_e64 s[4:5], s11, v2
	v_cmp_gt_u32_e64 s[6:7], s11, v3
	v_cmp_gt_u32_e64 s[12:13], s11, v4
	s_and_b64 s[4:5], s[56:57], s[4:5]
	s_and_b64 s[6:7], s[58:59], s[6:7]
	s_and_b64 s[12:13], s[60:61], s[12:13]
	v_cndmask_b32_e64 v25, v1, v25, s[4:5]
	v_cndmask_b32_e64 v27, v1, v27, s[6:7]
	v_cndmask_b32_e64 v64, v1, v64, s[12:13]
	v_add_u32_e32 v2, s73, v20
	v_add_u32_e32 v3, s88, v20
	v_add_u32_e32 v4, s89, v20
	v_cmp_gt_u32_e64 s[4:5], s11, v2
	v_cmp_gt_u32_e64 s[6:7], s11, v3
	v_cmp_gt_u32_e64 s[12:13], s11, v4
	s_and_b64 s[4:5], s[64:65], s[4:5]
	s_and_b64 s[6:7], s[66:67], s[6:7]
	s_and_b64 s[12:13], s[68:69], s[12:13]
	v_cndmask_b32_e64 v65, v1, v65, s[4:5]
	v_cndmask_b32_e64 v68, v1, v68, s[6:7]
	v_cndmask_b32_e64 v67, v1, v67, s[12:13]
	v_max3_f32 v0, v17, s14, v16
	v_max3_f32 v0, v0, v19, v18
	v_max3_f32 v0, v0, v22, v21
	v_max3_f32 v0, v0, v24, v23
	v_max3_f32 v0, v0, v26, v25
	v_max3_f32 v0, v0, v27, v64
	v_max3_f32 v0, v0, v66, v65
	v_max3_f32 v0, v0, v68, v67
	v_mov_b32_e32 v1, v0
	v_mov_b32_e32 v2, v0
	s_nop 1
	v_permlane32_swap_b32_e32 v1, v2
	v_cndmask_b32_e64 v1, v1, v2, s[36:37]
	v_max_f32_e32 v1, v1, v1
	v_max_f32_e32 v0, v0, v1
	s_or_b32 s86, s82, 8
	v_cmp_gt_f32_e32 vcc, v0, v140
	v_max_f32_e32 v1, v139, v139
	s_cmp_eq_u64 vcc, 0
	v_max_f32_e32 v1, v1, v0
	s_cselect_b64 vcc, -1, 0
	v_cndmask_b32_e32 v143, v1, v139, vcc
	v_sub_f32_e32 v16, v16, v143
	v_exp_f32_e32 v75, v16
	v_sub_f32_e32 v16, v19, v143
	v_sub_f32_e32 v2, v139, v1
	v_exp_f32_e32 v76, v16
	v_sub_f32_e32 v16, v18, v143
	v_exp_f32_e32 v2, v2
	v_exp_f32_e32 v77, v16
	v_sub_f32_e32 v16, v22, v143
	v_exp_f32_e32 v78, v16
	v_sub_f32_e32 v16, v21, v143
	v_exp_f32_e32 v79, v16
	v_sub_f32_e32 v16, v24, v143
	v_exp_f32_e32 v96, v16
	v_sub_f32_e32 v16, v23, v143
	v_mul_f32_e32 v0, 0, v2
	v_exp_f32_e32 v97, v16
	v_sub_f32_e32 v16, v26, v143
	v_cndmask_b32_e64 v0, v0, 0, vcc
	v_exp_f32_e32 v98, v16
	v_sub_f32_e32 v16, v25, v143
	v_cndmask_b32_e64 v69, v2, 1.0, vcc
	v_mov_b32_e32 v1, v0
	v_mov_b32_e32 v2, v0
	v_mov_b32_e32 v3, v0
	v_mov_b32_e32 v4, v0
	v_mov_b32_e32 v5, v0
	v_mov_b32_e32 v6, v0
	v_mov_b32_e32 v7, v0
	v_mov_b32_e32 v8, v0
	v_mov_b32_e32 v9, v0
	v_mov_b32_e32 v10, v0
	v_mov_b32_e32 v11, v0
	v_mov_b32_e32 v12, v0
	v_mov_b32_e32 v13, v0
	v_mov_b32_e32 v14, v0
	v_mov_b32_e32 v15, v0
	v_sub_f32_e32 v17, v17, v143
	v_exp_f32_e32 v99, v16
	v_sub_f32_e32 v16, v27, v143
	v_exp_f32_e32 v74, v17
	v_exp_f32_e32 v100, v16
	s_nop 1
	v_cvt_pk_bf16_f32 v70, v74, v75
	v_cvt_pk_bf16_f32 v71, v76, v77
	v_cvt_pk_bf16_f32 v72, v78, v79
	v_cvt_pk_bf16_f32 v73, v96, v97
	s_nop 1
	s_add_i32 s70, s82, 1
	s_waitcnt lgkmcnt(3)
	v_mfma_f32_32x32x16_bf16 v[16:31], v[44:47], v[70:73], v[0:15]
	v_sub_f32_e32 v44, v64, v143
	v_sub_f32_e32 v45, v66, v143
	v_sub_f32_e32 v46, v65, v143
	v_sub_f32_e32 v47, v68, v143
	v_exp_f32_e32 v44, v44
	v_exp_f32_e32 v45, v45
	v_exp_f32_e32 v46, v46
	s_waitcnt lgkmcnt(1)
	v_mfma_f32_32x32x16_bf16 v[0:15], v[40:43], v[70:73], v[0:15]
	v_sub_f32_e32 v40, v67, v143
	v_exp_f32_e32 v47, v47
	v_exp_f32_e32 v64, v40
	s_nop 1
	v_cvt_pk_bf16_f32 v40, v98, v99
	v_cvt_pk_bf16_f32 v41, v100, v44
	v_cvt_pk_bf16_f32 v42, v45, v46
	v_cvt_pk_bf16_f32 v43, v47, v64
	s_nop 1
	v_ashrrev_i32_e32 v95, 31, v94
	s_mov_b32 s87, 0
	v_mov_b32_e32 v145, v141
	s_waitcnt lgkmcnt(0)
	v_mfma_f32_32x32x16_bf16 v[0:15], v[32:35], v[40:43], v[0:15]
	v_add_f32_e32 v32, 0, v74
	v_add_f32_e32 v32, v75, v32
	v_add_f32_e32 v32, v76, v32
	v_add_f32_e32 v32, v77, v32
	v_add_f32_e32 v32, v78, v32
	v_add_f32_e32 v32, v79, v32
	v_add_f32_e32 v32, v96, v32
	v_add_f32_e32 v32, v97, v32
	v_add_f32_e32 v32, v98, v32
	v_mfma_f32_32x32x16_bf16 v[16:31], v[36:39], v[40:43], v[16:31]
	v_add_f32_e32 v32, v99, v32
	v_add_f32_e32 v32, v100, v32
	v_add_f32_e32 v32, v44, v32
	v_add_f32_e32 v32, v45, v32
	v_add_f32_e32 v32, v46, v32
	v_add_f32_e32 v32, v47, v32
	v_add_f32_e32 v144, v64, v32
	v_fmac_f32_e32 v144, v112, v69
	v_mov_b32_e32 v146, v142
	v_mov_b32_e32 v147, v87
	s_mov_b32 s83, s70
	s_branch .LBB0_354
